# speedup vs baseline: 1.0070x; 1.0070x over previous
_Z11main_kernelPKhPKfPf:
	s_load_dwordx4 s[12:15], s[0:1], 0x0
	s_load_dwordx2 s[10:11], s[0:1], 0x10
	s_bfe_u32 s4, s2, 0x50003
	s_sub_u32 s61, s4, 24
	s_cmp_lt_u32 s61, 4
	s_cselect_b32 s61, 1, 0
	s_lshl_b32 s62, s61, 2
	s_add_u32 s4, s4, s62
	s_cmp_gt_u32 s4, 27
	s_cselect_b64 s[16:17], -1, 0
	s_cmp_lt_u32 s4, 28
	v_readfirstlane_b32 s21, v0
	s_cselect_b64 s[6:7], -1, 0
	s_mov_b32 s28, 0
	s_and_b64 vcc, exec, s[16:17]
	s_mov_b32 s42, 0
	s_cmpk_ge_u32 s21, 0x180
	s_cselect_b64 s[74:75], 0, -1
	s_cselect_b32 s66, 0x180, 0
	s_cbranch_scc0 .Lred_ids
	v_subrev_u32_e32 v0, 0x180, v0
.Lred_ids:
	s_cbranch_vccnz .LBB1_6
	s_mov_b32 s1, 0
	s_cmp_lt_u32 s4, 7
	s_mov_b32 s0, s4
	s_cbranch_scc1 .LBB1_5
	s_mov_b32 s5, -8
	s_mov_b32 s1, 6
	s_mov_b32 s0, s4

.LBB1_50:
	s_sub_i32 s28, 0x7e, s31
	s_mul_i32 s28, s28, 6
	s_ashr_i32 s29, s28, 31
	s_add_u32 s26, s26, s28
	s_addc_u32 s27, s27, s29
	s_cmp_lg_u32 s41, 0
	s_cselect_b64 vcc, s[8:9], s[74:75]
	s_and_b64 vcc, exec, vcc
	s_cbranch_vccnz .LBB1_59
	s_cmp_lg_u32 s41, 0
	s_cbranch_scc0 .LBB1_55
	s_and_saveexec_b64 s[28:29], s[6:7]
	s_cbranch_execz .LBB1_54
	ds_read2_b32 v[34:35], v190 offset1:224
	ds_read2_b32 v[36:37], v237 offset1:224
	ds_read2_b32 v[38:39], v238 offset1:224
	ds_read2_b32 v[40:41], v239 offset1:224
	s_lshl_b32 s30, s56, 28
	s_add_i32 s30, s30, 0xa0000000
	s_ashr_i32 s30, s30, 31
	s_waitcnt lgkmcnt(3)
	v_add_f32_e32 v34, 0, v34
	v_add_f32_e32 v34, v34, v35
	s_waitcnt lgkmcnt(2)
	v_add_f32_e32 v34, v34, v36
	v_add_f32_e32 v34, v34, v37
	s_waitcnt lgkmcnt(1)
	v_add_f32_e32 v34, v34, v38
	v_add_f32_e32 v34, v34, v39
	s_waitcnt lgkmcnt(0)
	v_add_f32_e32 v34, v34, v40
	s_and_b32 s30, s30, 0x1800
	v_add_f32_e32 v34, v34, v41
	v_add_u32_e32 v35, s30, v232
	ds_write_b32 v35, v34 offset:256

.LBB1_76:
	s_add_i32 s57, s31, 1
	s_sub_i32 s28, 0x7d, s57
	s_mul_i32 s28, s28, 6
	s_ashr_i32 s29, s28, 31
	s_add_u32 s28, s26, s28
	s_addc_u32 s29, s27, s29
	s_cmp_lg_u32 s41, 0
	s_cselect_b64 vcc, s[8:9], s[74:75]
	s_and_b64 vcc, exec, vcc
	s_cbranch_vccnz .LBB1_85
	s_cmp_lg_u32 s41, 0
	s_cbranch_scc0 .LBB1_81
	s_and_saveexec_b64 s[26:27], s[6:7]
	s_cbranch_execz .LBB1_80
	ds_read2_b32 v[34:35], v216 offset1:224
	v_add_u32_e32 v36, 0x700, v216
	ds_read2_b32 v[36:37], v36 offset1:224
	v_add_u32_e32 v38, 0xe00, v216
	s_lshl_b32 s30, s56, 28
	s_waitcnt lgkmcnt(1)
	v_add_f32_e32 v34, 0, v34
	v_add_f32_e32 v40, v34, v35
	ds_read2_b32 v[34:35], v38 offset1:224
	v_add_u32_e32 v38, 0x1500, v216
	ds_read2_b32 v[38:39], v38 offset1:224
	s_waitcnt lgkmcnt(2)
	v_add_f32_e32 v36, v40, v36
	v_add_f32_e32 v36, v36, v37
	s_waitcnt lgkmcnt(1)
	v_add_f32_e32 v34, v36, v34
	s_add_i32 s30, s30, -2.0
	v_add_f32_e32 v34, v34, v35
	s_ashr_i32 s30, s30, 31
	s_waitcnt lgkmcnt(0)
	v_add_f32_e32 v34, v34, v38
	s_and_b32 s30, s30, 0x1800
	v_add_f32_e32 v34, v34, v39
	v_add_u32_e32 v35, s30, v232
	ds_write_b32 v35, v34 offset:512

.LBB1_110:
	s_add_i32 s34, s34, 1
	s_sub_i32 s30, 0x7d, s34
	s_mul_i32 s30, s30, 6
	s_ashr_i32 s31, s30, 31
	s_add_u32 s28, s28, s30
	s_addc_u32 s29, s29, s31
	s_cmp_lg_u32 s41, 0
	s_cselect_b64 vcc, s[8:9], s[74:75]
	s_and_b64 vcc, exec, vcc
	s_cbranch_vccnz .LBB1_119
	s_cmp_eq_u32 s41, 0
	s_cbranch_scc1 .LBB1_115
	s_and_saveexec_b64 s[30:31], s[6:7]
	s_cbranch_execz .LBB1_114
	ds_read2_b32 v[34:35], v190 offset1:224
	ds_read2_b32 v[36:37], v237 offset1:224
	ds_read2_b32 v[38:39], v238 offset1:224
	ds_read2_b32 v[40:41], v239 offset1:224
	s_lshl_b32 s35, s56, 28
	s_add_i32 s35, s35, 0xe0000000
	s_ashr_i32 s35, s35, 31
	s_waitcnt lgkmcnt(3)
	v_add_f32_e32 v34, 0, v34
	v_add_f32_e32 v34, v34, v35
	s_waitcnt lgkmcnt(2)
	v_add_f32_e32 v34, v34, v36
	v_add_f32_e32 v34, v34, v37
	s_waitcnt lgkmcnt(1)
	v_add_f32_e32 v34, v34, v38
	v_add_f32_e32 v34, v34, v39
	s_waitcnt lgkmcnt(0)
	v_add_f32_e32 v34, v34, v40
	s_and_b32 s35, s35, 0x1800
	v_add_f32_e32 v34, v34, v41
	v_add_u32_e32 v35, s35, v232
	ds_write_b32 v35, v34 offset:768

.LBB1_136:
	s_add_i32 s34, s34, 1
	s_sub_i32 s30, 0x7d, s34
	s_mul_i32 s30, s30, 6
	s_ashr_i32 s31, s30, 31
	s_add_u32 s30, s28, s30
	s_addc_u32 s31, s29, s31
	s_and_b64 s[28:29], exec, s[26:27]
	s_cselect_b32 s29, s52, s31
	s_cselect_b32 s28, s53, s30
	s_cselect_b32 s41, s49, s41
	s_cmp_lg_u32 s41, 0
	s_cselect_b64 vcc, s[8:9], s[74:75]
	s_and_b64 vcc, exec, vcc
	s_cbranch_vccnz .LBB1_145
	s_cmp_eq_u32 s41, 0
	s_cbranch_scc1 .LBB1_141
	s_and_saveexec_b64 s[30:31], s[6:7]
	s_cbranch_execz .LBB1_140
	ds_read2_b32 v[34:35], v216 offset1:224
	v_add_u32_e32 v36, 0x700, v216
	v_add_u32_e32 v38, 0xe00, v216
	ds_read2_b32 v[36:37], v36 offset1:224
	ds_read2_b32 v[38:39], v38 offset1:224
	s_bfe_i32 s35, s56, 0x10003
	s_waitcnt lgkmcnt(2)
	v_add_f32_e32 v34, 0, v34
	v_add_f32_e32 v40, v34, v35
	v_add_u32_e32 v34, 0x1500, v216
	ds_read2_b32 v[34:35], v34 offset1:224
	s_waitcnt lgkmcnt(2)
	v_add_f32_e32 v36, v40, v36
	v_add_f32_e32 v36, v36, v37
	s_waitcnt lgkmcnt(1)
	v_add_f32_e32 v36, v36, v38
	v_add_f32_e32 v36, v36, v39
	s_waitcnt lgkmcnt(0)
	v_add_f32_e32 v34, v36, v34
	s_and_b32 s35, s35, 0x1800
	v_add_f32_e32 v34, v34, v35
	v_add_u32_e32 v35, s35, v232
	ds_write_b32 v35, v34

.LBB1_164:
	s_sub_i32 s12, 0x7d, s30
	s_mul_i32 s12, s12, 6
	s_ashr_i32 s13, s12, 31
	s_add_u32 s12, s26, s12
	s_addc_u32 s13, s27, s13
	s_cmp_lg_u32 s41, 0
	s_cselect_b64 vcc, s[8:9], s[74:75]
	s_and_b64 vcc, exec, vcc
	s_cbranch_vccnz .LBB1_173
	s_cmp_lg_u32 s41, 0
	s_cbranch_scc0 .LBB1_169
	s_and_saveexec_b64 s[20:21], s[6:7]
	s_cbranch_execz .LBB1_168
	ds_read2_b32 v[34:35], v190 offset1:224
	v_add_u32_e32 v36, 0x700, v190
	v_add_u32_e32 v38, 0xe00, v190
	ds_read2_b32 v[36:37], v36 offset1:224
	ds_read2_b32 v[38:39], v38 offset1:224
	s_waitcnt lgkmcnt(2)
	v_add_f32_e32 v34, 0, v34
	v_add_f32_e32 v40, v34, v35
	v_add_u32_e32 v34, 0x1500, v190
	ds_read2_b32 v[34:35], v34 offset1:224
	s_waitcnt lgkmcnt(2)
	v_add_f32_e32 v36, v40, v36
	v_add_f32_e32 v36, v36, v37
	s_waitcnt lgkmcnt(1)
	v_add_f32_e32 v36, v36, v38
	v_add_f32_e32 v36, v36, v39
	s_waitcnt lgkmcnt(0)
	v_add_f32_e32 v34, v36, v34
	v_add_f32_e32 v34, v34, v35
	v_mov_b32_e32 v35, 0x19100
	v_lshl_add_u32 v35, v177, 2, v35
	ds_write_b32 v35, v34

.LBB1_190:
	s_sub_i32 s20, 0x7b, s30
	s_mul_i32 s20, s20, 6
	s_ashr_i32 s21, s20, 31
	s_add_u32 s12, s12, s20
	s_addc_u32 s13, s13, s21
	s_cmp_lg_u32 s41, 0
	s_cselect_b64 vcc, s[8:9], s[74:75]
	s_and_b64 vcc, exec, vcc
	s_cbranch_vccnz .LBB1_199
	s_cmp_lg_u32 s41, 0
	s_cbranch_scc0 .LBB1_195
	s_and_saveexec_b64 s[20:21], s[6:7]
	s_cbranch_execz .LBB1_194
	ds_read2_b32 v[34:35], v216 offset1:224
	v_add_u32_e32 v36, 0x700, v216
	v_add_u32_e32 v38, 0xe00, v216
	ds_read2_b32 v[36:37], v36 offset1:224
	ds_read2_b32 v[38:39], v38 offset1:224
	s_waitcnt lgkmcnt(2)
	v_add_f32_e32 v34, 0, v34
	v_add_f32_e32 v40, v34, v35
	v_add_u32_e32 v34, 0x1500, v216
	ds_read2_b32 v[34:35], v34 offset1:224
	s_waitcnt lgkmcnt(2)
	v_add_f32_e32 v36, v40, v36
	v_add_f32_e32 v36, v36, v37
	s_waitcnt lgkmcnt(1)
	v_add_f32_e32 v36, v36, v38
	v_add_f32_e32 v36, v36, v39
	s_waitcnt lgkmcnt(0)
	v_add_f32_e32 v34, v36, v34
	v_add_f32_e32 v34, v34, v35
	v_mov_b32_e32 v35, 0x19200
	v_lshl_add_u32 v35, v177, 2, v35
	ds_write_b32 v35, v34

.LBB1_216:
	s_sub_i32 s20, 0x79, s30
	s_mul_i32 s20, s20, 6
	s_ashr_i32 s21, s20, 31
	s_add_u32 s12, s12, s20
	s_addc_u32 s13, s13, s21
	s_cmp_lg_u32 s41, 0
	s_cselect_b64 vcc, s[8:9], s[74:75]
	s_and_b64 vcc, exec, vcc
	s_cbranch_vccnz .LBB1_225
	s_cmp_lg_u32 s41, 0
	s_cbranch_scc0 .LBB1_221
	s_and_saveexec_b64 s[20:21], s[6:7]
	s_cbranch_execz .LBB1_220
	ds_read2_b32 v[18:19], v190 offset1:224
	v_add_u32_e32 v20, 0x700, v190
	v_add_u32_e32 v22, 0xe00, v190
	ds_read2_b32 v[20:21], v20 offset1:224
	ds_read2_b32 v[22:23], v22 offset1:224
	s_waitcnt lgkmcnt(2)
	v_add_f32_e32 v18, 0, v18
	v_add_f32_e32 v24, v18, v19
	v_add_u32_e32 v18, 0x1500, v190
	ds_read2_b32 v[18:19], v18 offset1:224
	s_waitcnt lgkmcnt(2)
	v_add_f32_e32 v20, v24, v20
	v_add_f32_e32 v20, v20, v21
	s_waitcnt lgkmcnt(1)
	v_add_f32_e32 v20, v20, v22
	v_add_f32_e32 v20, v20, v23
	s_waitcnt lgkmcnt(0)
	v_add_f32_e32 v18, v20, v18
	v_add_f32_e32 v18, v18, v19
	v_mov_b32_e32 v19, 0x19300
	v_lshl_add_u32 v19, v177, 2, v19
	ds_write_b32 v19, v18

.LBB1_235:
	v_add_u32_e32 v0, s66, v0
	v_subrev_u32_e32 v0, 0x100, v0
	s_movk_i32 s0, 0xf0
	v_cmp_gt_u32_e32 vcc, s0, v0
	s_and_saveexec_b64 s[0:1], vcc
	s_cbranch_execz .Lepi_idle
	s_movk_i32 s0, 0x77
	v_mov_b32_e32 v1, 0xffffff88
	v_cmp_lt_u32_e32 vcc, s0, v0
	v_mov_b32_e32 v2, 0x44704000
	s_mov_b32 s0, 0xf800000
	v_cndmask_b32_e32 v1, 0, v1, vcc
	v_add_u32_e32 v0, v1, v0
	v_cvt_f32_u32_e32 v1, v0
	s_mov_b32 s5, 0x17800
	s_mov_b32 s4, 0x3eb17218
	v_fmac_f32_e32 v2, 0xc1000000, v1
	v_mul_f32_e32 v1, 0x4f800000, v2
	v_cmp_gt_f32_e64 s[0:1], s0, v2
	s_nop 1
	v_cndmask_b32_e64 v1, v2, v1, s[0:1]
	v_sqrt_f32_e32 v2, v1
	s_nop 0
	v_add_u32_e32 v3, -1, v2
	v_fma_f32 v4, -v3, v2, v1
	v_cmp_ge_f32_e64 s[2:3], 0, v4
	v_add_u32_e32 v4, 1, v2
	s_nop 0
	v_cndmask_b32_e64 v3, v2, v3, s[2:3]
	v_fma_f32 v2, -v4, v2, v1
	v_cmp_lt_f32_e64 s[2:3], 0, v2
	s_nop 1
	v_cndmask_b32_e64 v2, v3, v4, s[2:3]
	v_mul_f32_e32 v3, 0x37800000, v2
	v_cndmask_b32_e64 v2, v2, v3, s[0:1]
	v_mov_b32_e32 v3, 0x260
	v_cmp_class_f32_e64 s[0:1], v1, v3
	s_nop 1
	v_cndmask_b32_e64 v1, v2, v1, s[0:1]
	v_sub_f32_e32 v1, 0x41f80000, v1
	v_mul_f32_e32 v1, 0.5, v1
	v_cvt_i32_f32_e32 v1, v1
	s_and_b64 s[0:1], exec, s[16:17]
	s_cselect_b32 s2, s40, s38
	s_cselect_b32 s3, s39, s33
	v_sub_u32_e32 v2, 31, v1
	v_mul_lo_u32 v2, v2, v1
	v_lshrrev_b32_e32 v3, 31, v2
	v_add_u32_e32 v2, v2, v3
	v_ashrrev_i32_e32 v2, 1, v2
	v_cmp_gt_i32_e64 s[0:1], v2, v0
	s_nop 1
	v_subbrev_co_u32_e64 v1, s[0:1], 0, v1, s[0:1]
	v_add_u32_e32 v2, 1, v1
	v_sub_u32_e32 v3, 30, v1
	v_mul_lo_u32 v3, v2, v3
	v_lshrrev_b32_e32 v4, 31, v3
	v_add_u32_e32 v3, v3, v4
	v_ashrrev_i32_e32 v3, 1, v3
	v_cmp_gt_i32_e64 s[0:1], v3, v0
	s_nop 1
	v_cndmask_b32_e64 v12, v2, v1, s[0:1]
	v_sub_u32_e32 v1, 31, v12
	v_mul_lo_u32 v1, v1, v12
	v_lshrrev_b32_e32 v2, 31, v1
	v_add_u32_e32 v1, v1, v2
	v_ashrrev_i32_e32 v1, 1, v1
	v_sub_u32_e32 v0, v0, v1
	v_cndmask_b32_e64 v1, 0, 16, vcc
	v_lshl_or_b32 v1, s2, 5, v1
	v_add_u32_e32 v1, v1, v12
	v_sub_u32_e32 v2, 0xff, v1
	v_mul_lo_u32 v1, v2, v1
	v_lshrrev_b32_e32 v2, 31, v1
	v_add_u32_e32 v1, v1, v2
	v_ashrrev_i32_e32 v1, 1, v1
	v_add3_u32 v13, v12, v0, 1
	v_add_u32_e32 v0, v1, v0
	v_ashrrev_i32_e32 v1, 31, v0
	v_mov_b32_e32 v2, 0x1fc0
	v_mad_u64_u32 v[0:1], s[0:1], s3, v2, v[0:1]
	v_mad_u64_u32 v[4:5], s[0:1], v0, 24, s[10:11]
	v_mov_b32_e32 v0, 0x17800
	v_lshl_add_u32 v14, v12, 2, v0
	v_mov_b32_e32 v0, 0x60
	v_cndmask_b32_e32 v15, 0, v0, vcc
	v_or_b32_e32 v2, 16, v15
	v_add_lshl_u32 v3, v2, v12, 6
	v_add_u32_e32 v2, v2, v13
	v_lshl_add_u32 v6, v2, 6, v14
	v_add_u32_e32 v2, 32, v15
	v_add_lshl_u32 v7, v2, v12, 6
	v_add_u32_e32 v2, v2, v13
	v_lshl_add_u32 v8, v2, 6, v14
	v_add_u32_e32 v2, 48, v15
	v_mad_i32_i24 v5, v1, 24, v5
	v_add_lshl_u32 v0, v15, v12, 6
	v_lshlrev_b32_e32 v16, 2, v13
	v_add_u32_e32 v1, v15, v13
	v_add_lshl_u32 v9, v2, v12, 6
	v_add_u32_e32 v17, 64, v15
	v_add_u32_e32 v15, 0x50, v15
	v_add3_u32 v0, v0, v16, s5
	v_lshl_add_u32 v1, v1, 6, v14
	v_add3_u32 v3, v3, v16, s5
	v_add3_u32 v7, v7, v16, s5
	v_add3_u32 v9, v9, v16, s5
	v_add_u32_e32 v2, v2, v13
	v_add_lshl_u32 v18, v17, v12, 6
	v_add_lshl_u32 v12, v15, v12, 6
	s_load_dwordx4 s[0:3], s[14:15], 0x0
	v_lshl_add_u32 v10, v2, 6, v14
	ds_read_b32 v0, v0
	ds_read_b32 v2, v1
	ds_read_b32 v1, v3
	ds_read_b32 v3, v6
	ds_read_b32 v6, v7
	ds_read_b32 v8, v8
	ds_read_b32 v7, v9
	ds_read_b32 v9, v10
	v_add3_u32 v18, v18, v16, s5
	v_add3_u32 v16, v12, v16, s5
	v_add_u32_e32 v12, v15, v13
	v_add_u32_e32 v17, v17, v13
	v_lshl_add_u32 v15, v12, 6, v14
	s_load_dwordx2 s[6:7], s[14:15], 0x10
	v_lshl_add_u32 v17, v17, 6, v14
	ds_read_b32 v12, v18
	ds_read_b32 v14, v17
	ds_read_b32 v13, v16
	ds_read_b32 v15, v15
	s_waitcnt lgkmcnt(0)
	v_pk_add_f32 v[0:1], v[0:1], v[2:3]
	v_mov_b32_e32 v2, s2
	v_mov_b32_e32 v3, s3
	v_mov_b64_e32 v[10:11], s[0:1]
	v_pk_add_f32 v[6:7], v[6:7], v[8:9]
	v_pk_fma_f32 v[0:1], v[0:1], s[4:5], v[10:11] op_sel_hi:[1,0,1]
	v_pk_fma_f32 v[2:3], v[6:7], s[4:5], v[2:3] op_sel_hi:[1,0,1]
	global_store_dwordx4 v[4:5], v[0:3], off
	s_nop 1
	v_pk_add_f32 v[0:1], v[12:13], v[14:15]
	v_mov_b64_e32 v[2:3], s[6:7]
	v_pk_fma_f32 v[0:1], v[0:1], s[4:5], v[2:3] op_sel_hi:[1,0,1]
	global_store_dwordx2 v[4:5], v[0:1], off offset:16
	s_endpgm
